# layer-0 in-proj phase gets staggered conversion slots (WGs 0-127 one item per wave at phase start, WGs 128-255 a second item in the idle tail); prologue keeps 6656 expert items
# speedup vs baseline: 1.0052x; 1.0052x over previous
.LBB0_41:
	v_writelane_b32 v253, s24, 32
	v_writelane_b32 v253, s23, 34
	v_writelane_b32 v253, s22, 36
	s_mov_b32 s3, 0
	v_readlane_b32 s0, v253, 29
	s_lshl_b32 s0, s0, 14
	s_add_i32 s29, s0, 0
	s_cmp_lg_u64 s[48:49], 0
	v_readlane_b32 s4, v253, 30
	s_cselect_b64 s[44:45], -1, 0
	s_abs_i32 s2, s4
	v_cvt_f32_u32_e32 v2, s2
	s_sub_i32 s0, 0, s2
	s_ashr_i32 s6, s4, 31
	v_rcp_iflag_f32_e32 v2, v2
	s_nop 0
	v_mul_f32_e32 v2, 0x4f7ffffe, v2
	v_cvt_u32_f32_e32 v2, v2
	s_nop 0
	v_readfirstlane_b32 s1, v2
	s_mul_i32 s0, s0, s1
	s_mul_hi_u32 s0, s1, s0
	s_add_i32 s7, s1, s0
	s_mul_hi_u32 s0, s7, 0x4200
	s_mul_i32 s0, s0, s2
	s_sub_i32 s0, 0x4200, s0
	s_sub_i32 s1, s0, s2
	s_cmp_ge_u32 s0, s2
	s_cselect_b32 s0, s1, s0
	s_sub_i32 s1, s0, s2
	s_cmp_ge_u32 s0, s2
	s_cselect_b32 s8, s1, s0
	s_add_i32 s0, s4, 0xffffff00
	s_cmp_ge_i32 s0, s8
	s_cselect_b64 s[0:1], -1, 0
	s_cmpk_lt_u32 s8, 0x2101
	s_cselect_b64 s[4:5], -1, 0
	s_sub_i32 s8, 0x4200, s8
	s_and_b64 s[0:1], s[0:1], s[4:5]
	s_and_b64 s[0:1], s[0:1], exec
	s_cselect_b32 s5, s8, 0x4200
	s_add_i32 s0, s5, 0xffffda00
	s_cmp_eq_u32 s2, 0x800
	s_cselect_b32 s5, s0, s5
	v_writelane_b32 v253, s5, 38
	v_writelane_b32 v253, s48, 40
	s_mul_hi_u32 s0, s5, s7
	s_mul_i32 s1, s0, s2
	v_writelane_b32 v253, s49, 41
	v_writelane_b32 v253, s50, 42
	v_writelane_b32 v253, s51, 43
	v_writelane_b32 v253, s52, 44
	v_writelane_b32 v253, s53, 45
	v_writelane_b32 v253, s54, 46
	v_writelane_b32 v253, s55, 47
	s_sub_i32 s1, s5, s1
	v_writelane_b32 v253, s56, 48
	s_add_i32 s4, s0, 1
	s_sub_i32 s5, s1, s2
	v_writelane_b32 v253, s57, 49
	s_cmp_ge_u32 s1, s2
	v_writelane_b32 v253, s58, 50
	s_cselect_b32 s0, s4, s0
	v_writelane_b32 v253, s59, 51
	s_cselect_b32 s1, s5, s1
	s_add_i32 s4, s0, 1
	v_writelane_b32 v253, s60, 52
	s_cmp_ge_u32 s1, s2
	v_writelane_b32 v253, s61, 53
	s_cselect_b32 s0, s4, s0
	v_writelane_b32 v253, s62, 54
	s_xor_b32 s0, s0, s6
	v_writelane_b32 v253, s63, 55
	s_sub_i32 s15, s0, s6
	v_writelane_b32 v253, s29, 56
	s_add_i32 s14, s15, -1
	v_writelane_b32 v253, s44, 57
	s_cmp_lt_i32 s15, 1
	v_readfirstlane_b32 s0, v0
	v_writelane_b32 v253, s45, 58
	s_cbranch_scc1 .LBB0_65
	s_ashr_i32 s0, s0, 6
	s_min_i32 s18, s0, s14
	s_cmpk_gt_i32 s27, 0x7ff
	v_readlane_b32 s0, v253, 26
	s_cselect_b64 s[20:21], -1, 0
	s_add_u32 s0, s0, 0x800000
	v_writelane_b32 v253, s0, 59
	v_mov_b32_e32 v133, 0
	v_readlane_b32 s0, v253, 27
	s_addc_u32 s0, s0, 0
	s_add_i32 s25, 0, 0x21000
	v_writelane_b32 v253, s0, 61
	s_add_i32 s0, 0, 0x21200
	v_writelane_b32 v253, s0, 63
	s_add_i32 s0, 0, 0x21100
	v_writelane_b32 v254, s0, 1
	s_add_i32 s0, 0, 0x21300
	v_writelane_b32 v254, s0, 3
	v_writelane_b32 v254, s27, 5
	v_writelane_b32 v254, s14, 7
	v_writelane_b32 v254, s15, 9
	v_writelane_b32 v254, s18, 11
	v_writelane_b32 v254, s20, 13
	s_mov_b32 s22, 0x42800000
	s_mov_b32 s19, 0
	v_writelane_b32 v254, s21, 14
	s_branch .LBB0_45

.LBB0_243:
	s_or_b64 exec, exec, s[30:31]
	s_mul_i32 s0, s36, 0x11400000
	s_add_i32 s97, s0, 0x800000
	s_waitcnt vmcnt(2)
	v_mov_b32_e32 v10, v0
	s_mov_b64 s[0:1], 0
	s_mov_b32 s28, s37
	v_readlane_b32 s29, v253, 8
	s_waitcnt lgkmcnt(0)
	s_barrier
	v_readlane_b32 s1, v253, 9
	s_cmpk_lg_i32 s1, 0x100
	s_cbranch_scc1 .Lfs5_skip
	v_readlane_b32 s1, v254, 20
	s_cmp_eq_u32 s1, 0
	s_cbranch_scc1 .Lfs5_skip
	s_cmpk_gt_i32 s29, 0x7f
	s_cbranch_scc1 .Lfs5_skip
	v_readfirstlane_b32 s1, v0
	s_lshl_b32 s0, s29, 3
	s_lshr_b32 s1, s1, 6
	s_add_i32 s0, s0, s1
	s_addk_i32 s0, 0x1e00
	s_mov_b32 s101, 5
	v_readlane_b32 s62, v253, 54
	v_readlane_b32 s26, v253, 55
	s_mov_b32 s73, 0x10000
	v_mov_b32_e32 v135, v0
	v_and_b32_e32 v132, 63, v0
	s_branch .Ltkf_go

.Lfs5_skip:
	v_mov_b32_e32 v10, v0
	s_mov_b64 s[0:1], 0
	s_mov_b32 s28, s37
	v_readlane_b32 s29, v253, 8
	s_cmpk_gt_i32 s29, 0x57f
	v_readfirstlane_b32 s3, v10
	s_cbranch_scc1 .LBB0_269
	s_waitcnt vmcnt(0)
	v_bfe_i32 v4, v10, 27, 1
	v_lshlrev_b32_e32 v2, 4, v10
	v_lshrrev_b32_e32 v4, 22, v4
	v_add_u32_e32 v4, v2, v4
	v_and_b32_e32 v4, 0xfffffc00, v4
	v_sub_u32_e32 v4, v2, v4
	v_ashrrev_i32_e32 v3, 31, v10
	v_lshrrev_b32_e32 v5, 4, v4
	v_lshrrev_b32_e32 v3, 26, v3
	v_bitop3_b32 v4, v5, v4, 32 bitop3:0x6c
	v_add_u32_e32 v3, v10, v3
	v_ashrrev_i32_e32 v6, 31, v4
	v_ashrrev_i32_e32 v3, 6, v3
	v_lshrrev_b32_e32 v6, 26, v6
	v_lshlrev_b32_e32 v5, 3, v3
	v_add_u32_e32 v6, v4, v6
	v_readlane_b32 s4, v253, 40
	v_and_b32_e32 v5, -16, v5
	v_ashrrev_i32_e32 v7, 6, v6
	v_and_b32_e32 v6, 0xc0, v6
	v_readlane_b32 s16, v253, 52
	v_readlane_b32 s18, v253, 54
	v_add_u32_e32 v5, v7, v5
	v_sub_u32_e32 v4, v4, v6
	s_add_u32 s16, s18, s0
	v_lshlrev_b32_e32 v3, 5, v3
	v_ashrrev_i16_sdwa v4, v237, sext(v4) dst_sel:DWORD dst_unused:UNUSED_PAD src0_sel:DWORD src1_sel:BYTE_0
	v_lshlrev_b32_e32 v6, 1, v5
	v_lshrrev_b32_e32 v8, 2, v5
	v_and_b32_e32 v7, 3, v7
	s_mov_b32 s0, 0x1fffe0
	v_and_b32_e32 v3, 32, v3
	v_bfe_i32 v4, v4, 0, 16
	v_and_b32_e32 v6, 24, v6
	v_and_b32_e32 v8, 4, v8
	v_and_or_b32 v7, v5, s0, v7
	v_or3_b32 v6, v7, v8, v6
	v_add_lshl_u32 v3, v3, v4, 1
	v_add_u32_e32 v2, 0x2000, v2
	v_lshl_add_u32 v194, v5, 11, v3
	v_lshl_add_u32 v130, v6, 11, v3
	v_ashrrev_i32_e32 v3, 31, v2
	v_lshrrev_b32_e32 v3, 22, v3
	v_add_u32_e32 v3, v2, v3
	v_ashrrev_i32_e32 v3, 10, v3
	v_mul_i32_i24_e32 v4, 0x400, v3
	v_sub_u32_e32 v2, v2, v4
	v_lshrrev_b32_e32 v4, 4, v2
	v_readlane_b32 s17, v253, 53
	v_readlane_b32 s19, v253, 55
	v_bitop3_b32 v2, v4, v2, 32 bitop3:0x6c
	s_addc_u32 s17, s19, s1
	v_ashrrev_i32_e32 v5, 31, v2
	s_add_u32 s30, s16, 0x23000000
	v_lshrrev_b32_e32 v5, 26, v5
	s_addc_u32 s31, s17, 0
	v_lshlrev_b32_e32 v4, 3, v3
	v_add_u32_e32 v5, v2, v5
	s_add_u32 s37, s16, s97
	v_and_b32_e32 v4, -16, v4
	v_ashrrev_i32_e32 v6, 6, v5
	s_addc_u32 s38, s17, 0
	v_add_u32_e32 v4, v6, v4
	v_and_b32_e32 v6, 3, v6
	s_ashr_i32 s39, s29, 31
	v_and_or_b32 v6, v4, s0, v6
	s_lshr_b32 s0, s39, 29
	s_add_i32 s0, s29, s0
	v_readlane_b32 s6, v253, 42
	s_ashr_i32 s19, s3, 6
	s_ashr_i32 s1, s0, 3
	s_and_b32 s0, s0, -8
	s_ashr_i32 s18, s3, 8
	s_lshl_b32 s6, s19, 10
	s_sub_i32 s0, s29, s0
	s_cmp_lt_i32 s0, 0
	s_movk_i32 s2, 0xb1
	s_cselect_b32 s2, s2, 0xb0
	s_mul_i32 s0, s2, s0
	s_add_i32 s0, s0, s1
	s_mul_hi_i32 s1, s0, 0x2e8ba2e9
	s_lshr_b32 s2, s1, 31
	s_ashr_i32 s1, s1, 3
	s_add_i32 s1, s1, s2
	s_lshl_b32 s4, s1, 2
	s_mul_i32 s1, s1, 44
	s_sub_i32 s0, s0, s1
	s_bfe_i32 s1, s0, 0x80000
	s_bfe_u32 s1, s1, 0x2000d
	s_add_i32 s1, s0, s1
	s_bfe_i32 s2, s1, 0x80000
	s_and_b32 s1, s1, 0xfc
	s_sub_i32 s0, s0, s1
	s_sext_i32_i8 s0, s0
	s_add_i32 s24, s4, s0
	s_sext_i32_i16 s2, s2
	s_ashr_i32 s25, s24, 31
	s_lshr_b32 s2, s2, 2
	s_lshl_b64 s[0:1], s[24:25], 19
	v_readlane_b32 s5, v253, 41
	s_add_u32 s0, s30, s0
	s_addc_u32 s1, s31, s1
	s_bfe_i64 s[4:5], s[2:3], 0x100000
	v_and_b32_e32 v5, 0xc0, v5
	s_lshl_b64 s[4:5], s[4:5], 19
	v_sub_u32_e32 v2, v2, v5
	s_add_u32 s4, s37, s4
	v_lshlrev_b32_e32 v3, 5, v3
	v_ashrrev_i16_sdwa v2, v237, sext(v2) dst_sel:DWORD dst_unused:UNUSED_PAD src0_sel:DWORD src1_sel:BYTE_0
	v_lshlrev_b32_e32 v5, 1, v4
	v_lshrrev_b32_e32 v7, 2, v4
	s_addc_u32 s5, s38, s5
	s_add_i32 s40, s6, 0
	v_and_b32_e32 v3, 32, v3
	v_bfe_i32 v2, v2, 0, 16
	v_and_b32_e32 v5, 24, v5
	v_and_b32_e32 v7, 4, v7
	s_add_i32 s41, s40, 0x10000
	s_add_i32 s42, s40, 0x12000
	v_readlane_b32 s7, v253, 43
	v_or3_b32 v5, v6, v7, v5
	v_add_lshl_u32 v2, v3, v2, 1
	s_mov_b32 m0, s41
	s_add_u32 s6, s4, 0x40000
	v_lshl_add_u32 v134, v5, 11, v2
	global_load_lds_dwordx4 v130, s[4:5]
	s_mov_b32 m0, s42
	s_addc_u32 s7, s5, 0
	s_add_i32 s43, s40, 0x14000
	global_load_lds_dwordx4 v134, s[4:5]
	s_mov_b32 m0, s43
	s_add_i32 s44, s40, 0x16000
	global_load_lds_dwordx4 v130, s[6:7]
	s_mov_b32 m0, s44
	s_add_i32 s45, s40, 0x2000
	global_load_lds_dwordx4 v134, s[6:7]
	s_mov_b32 m0, s40
	s_add_u32 s6, s0, 0x40000
	v_lshl_add_u32 v132, v4, 11, v2
	global_load_lds_dwordx4 v194, s[0:1]
	s_mov_b32 m0, s45
	s_addc_u32 s7, s1, 0
	s_add_i32 s46, s40, 0x4000
	global_load_lds_dwordx4 v132, s[0:1]
	s_mov_b32 m0, s46
	s_add_i32 s47, s40, 0x6000
	global_load_lds_dwordx4 v194, s[6:7]
	s_mov_b32 m0, s47
	v_mov_b32_e32 v131, v195
	global_load_lds_dwordx4 v132, s[6:7]
	v_mov_b32_e32 v135, v195
	v_mov_b32_e32 v133, v195
	s_cmp_eq_u32 s18, 1
	v_lshl_add_u64 v[8:9], s[4:5], 0, v[130:131]
	v_lshl_add_u64 v[6:7], s[4:5], 0, v[134:135]
	v_lshl_add_u64 v[2:3], s[0:1], 0, v[194:195]
	s_cselect_b64 s[6:7], -1, 0
	s_cmp_lg_u32 s18, 1
	v_lshl_add_u64 v[4:5], s[0:1], 0, v[132:133]
	v_readlane_b32 s8, v253, 44
	v_readlane_b32 s9, v253, 45
	v_readlane_b32 s10, v253, 46
	v_readlane_b32 s11, v253, 47
	v_readlane_b32 s12, v253, 48
	v_readlane_b32 s13, v253, 49
	v_readlane_b32 s14, v253, 50
	v_readlane_b32 s15, v253, 51
	s_cbranch_scc1 .LBB0_246
	s_barrier

.Lfill_done:
	v_readlane_b32 s1, v253, 9
	s_cmpk_lg_i32 s1, 0x100
	s_cbranch_scc1 .Lfs6_skip
	v_readlane_b32 s1, v254, 20
	s_cmp_eq_u32 s1, 0
	s_cbranch_scc1 .Lfs6_skip
	v_readlane_b32 s27, v253, 8
	s_cmpk_lt_i32 s27, 0x80
	s_cbranch_scc1 .Lfs6_skip
	v_readfirstlane_b32 s1, v0
	s_lshl_b32 s0, s27, 3
	s_lshr_b32 s1, s1, 6
	s_add_i32 s0, s0, s1
	s_addk_i32 s0, 0x1600
	s_mov_b32 s101, 6
	v_readlane_b32 s62, v253, 54
	v_readlane_b32 s26, v253, 55
	s_mov_b32 s73, 0x10000
	v_mov_b32_e32 v135, v0
	v_and_b32_e32 v132, 63, v0
	s_branch .Ltkf_go
.Lfret_6:
	s_mov_b32 s101, 0
	s_waitcnt vmcnt(0) lgkmcnt(0)
.Lfs6_skip:
.LBB0_298:
	s_getreg_b32 s0, hwreg(HW_REG_XCC_ID, 0, 4)
	s_waitcnt vmcnt(0)
	s_waitcnt vmcnt(0) lgkmcnt(0)
	s_barrier
	s_mov_b64 s[2:3], exec
	v_readlane_b32 s4, v253, 4
	v_readlane_b32 s5, v253, 5
	s_and_b64 s[4:5], s[2:3], s[4:5]
	s_xor_b64 s[30:31], s[4:5], s[2:3]
	s_mov_b64 exec, s[4:5]
	s_cbranch_execz .LBB0_352
	v_readlane_b32 s1, v254, 24
	s_waitcnt vmcnt(0) expcnt(0) lgkmcnt(0)
	s_and_b32 s37, s0, 15
	v_mov_b32_e32 v2, s1
	ds_read_b32 v4, v2
	v_readlane_b32 s1, v254, 17
	s_waitcnt lgkmcnt(0)
	v_cmp_ne_u32_e32 vcc, 0, v4
	v_mov_b32_e32 v2, s1
	ds_read_b32 v2, v2
	s_cbranch_vccnz .LBB0_315
	v_readlane_b32 s2, v253, 0
	v_readlane_b32 s3, v253, 1
	s_load_dwordx2 s[0:1], s[2:3], 0x4
	v_readlane_b32 s2, v253, 9
	s_mov_b32 s16, 1
	s_waitcnt lgkmcnt(0)
	s_mul_i32 s17, s0, s2
	s_mul_i32 s17, s17, s1
	s_mov_b64 s[0:1], 0
	s_branch .LBB0_303
